# phase 10 token-table build: the ten STOK loads pipelined, one wait + LDS writes at the end; on top of v39
# speedup vs baseline: 1.0055x; 1.0005x over previous
; #define LAS __attribute__((address_space(3)))
; __device__ __forceinline__ int fresh_lane() { int l; asm volatile("v_mbcnt_lo_u32_b32 %0, -1, 0\n\tv_mbcnt_hi_u32_b32 %0, -1, %0" : "=v"(l)); return l; }
;     __device__ __forceinline__ bool next(int i, Unit& u) const {
;         if (i + i0 >= imax) return false; const long L = (long)(i + i0) * G + c; if (L >= nwg) return false;
;         int wgid = (int)L; { const int q = nwg / NXCD, r = nwg % NXCD, xcd = wgid % NXCD, off = wgid / NXCD; wgid = (xcd < r ? xcd * (q + 1) : r * (q + 1) + (xcd - r) * q) + off; }
;         const int tq = wgid / nN, e = tile_e[tq], ft = tile_e[256 + e] >> 8, gsz = (tile_e[320 + e] + 255) >> 8, idx = wgid - ft * nN;
;         u.pm = ft + idx % gsz; u.pn = idx / gsz; u.e = e; return true;
; __global__ void __launch_bounds__(NWAVES * 64, 2) mk_fwd(Args args) {
;     ...
;         const LAS int* tile_e = (const LAS int*)(lds + TILE_OFF); const int nTiles = tile_e[160];
;         pg8::Gemm g{(const pg8::bf16_t*)(ws + WS_H), (const pg8::bf16_t*)(ws + WS_WUP), nTiles * 256, 4096, 2048, (size_t)4096 * 2048 * 2, 1};
;         pg8::MoeOrder<true> S; S.init(nTiles, 4096, G, bid, tile_e); S.tab = (const LAS int*)(lds + TOKTAB_OFF);
;         { const int tid = wave * 64 + fresh_lane(); const int* STOK = (const int*)(ws + WS_STOK); LAS int* tab = (LAS int*)(lds + TOKTAB_OFF);
;           const LAS int* pstart = (const LAS int*)(lds + TILE_OFF + 1024); const LAS int* etot = (const LAS int*)(lds + TILE_OFF + 1280);
;           for (int i = 0; i < 10; ++i) { pg8::Unit u; if (!S.next(i, u)) break;
;               if (tid < 256) { const int rr = u.pm * 256 + tid - pstart[u.e]; const bool valid = rr < etot[u.e]; tab[i * 256 + tid] = valid ? STOK[u.e * 8192 + rr] : 0; } }
;           __syncthreads(); }
.LBB0_2139:
	s_or_b64 exec, exec, s[2:3]
	s_add_i32 s3, 0, 0x26e80
	v_mov_b32_e32 v0, s3
	s_waitcnt lgkmcnt(0)
	s_barrier
	ds_read_b32 v0, v0
	s_ashr_i32 s62, s81, 31
	s_lshr_b32 s2, s62, 29
	s_add_i32 s2, s81, s2
	s_and_b32 s3, s2, -8
	s_ashr_i32 s18, s2, 3
	s_waitcnt lgkmcnt(0)
	v_readfirstlane_b32 s2, v0
	s_lshl_b32 s10, s2, 4
	s_ashr_i32 s17, s16, 31
	s_sub_i32 s5, s81, s3
	s_ashr_i32 s11, s10, 31
	s_ashr_i32 s63, s10, 3
	s_cmp_lt_i32 s81, s10
	s_cselect_b64 s[28:29], -1, 0
	s_cmp_ge_i32 s81, s10
	v_mbcnt_lo_u32_b32 v0, -1, 0
	v_mbcnt_hi_u32_b32 v0, -1, v0
	s_cbranch_scc1 .LBB0_2190
	s_add_u32 s14, s8, 0x600000
	v_add_u32_e32 v1, s33, v0
	s_addc_u32 s15, s9, 0
	s_add_i32 s2, 0, 0x20000
	v_lshl_add_u32 v0, v1, 2, s2
	s_movk_i32 s2, 0x100
	v_cmp_gt_i32_e64 s[2:3], s2, v1
	s_and_saveexec_b64 s[26:27], s[2:3]
	s_cbranch_execz .LBB0_2144
	s_lshr_b32 s4, s5, 31
	s_or_b32 s4, s63, s4
	s_mul_i32 s4, s4, s5
	s_add_i32 s4, s4, s18
	s_ashr_i32 s19, s4, 31
	s_lshr_b32 s19, s19, 28
	s_add_i32 s19, s4, s19
	s_ashr_i32 s19, s19, 4
	s_lshl_b32 s19, s19, 2
	s_add_i32 s20, 0, 0x26c00
	s_add_i32 s19, s20, s19
	v_mov_b32_e32 v2, s19
	ds_read_b32 v2, v2
	s_waitcnt lgkmcnt(0)
	v_lshlrev_b32_e32 v3, 2, v2
	v_add_u32_e32 v3, s20, v3
	ds_read2st64_b32 v[4:5], v3 offset0:4 offset1:5
	s_waitcnt lgkmcnt(0)
	v_readfirstlane_b32 s19, v5
	s_addk_i32 s19, 0xff
	s_ashr_i32 s19, s19, 8
	s_abs_i32 s19, s19
	v_cvt_f32_u32_e32 v3, s19
	v_readfirstlane_b32 s20, v4
	s_ashr_i32 s20, s20, 8
	s_sub_i32 s22, 0, s19
	v_rcp_iflag_f32_e32 v3, v3
	s_lshl_b32 s21, s20, 4
	s_sub_i32 s4, s4, s21
	s_ashr_i32 s21, s4, 31
	v_mul_f32_e32 v3, 0x4f7ffffe, v3
	v_cvt_u32_f32_e32 v3, v3
	s_abs_i32 s4, s4
	v_readfirstlane_b32 s23, v3
	s_mul_i32 s22, s22, s23
	s_mul_hi_u32 s22, s23, s22
	s_add_i32 s23, s23, s22
	s_mul_hi_u32 s22, s4, s23
	s_mul_i32 s22, s22, s19
	s_sub_i32 s4, s4, s22
	s_sub_i32 s22, s4, s19
	s_cmp_ge_u32 s4, s19
	s_cselect_b32 s4, s22, s4
	s_sub_i32 s22, s4, s19
	s_cmp_ge_u32 s4, s19
	s_cselect_b32 s4, s22, s4
	s_xor_b32 s4, s4, s21
	s_sub_i32 s4, s4, s21
	s_add_i32 s4, s4, s20
	v_lshl_add_u32 v3, s4, 8, v1
	v_sub_u32_e32 v4, v3, v4
	v_cmp_lt_i32_e32 vcc, v4, v5
	v_mov_b32_e32 v20, 0
	s_and_saveexec_b64 s[30:31], vcc
	s_cbranch_execz .LBB0_2143
	v_lshl_add_u32 v2, v2, 13, v4
	v_ashrrev_i32_e32 v3, 31, v2
	v_lshl_add_u64 v[2:3], v[2:3], 2, s[14:15]
	global_load_dword v20, v[2:3], off

;     __device__ __forceinline__ bool next(int i, Unit& u) const {
;         if (i + i0 >= imax) return false; const long L = (long)(i + i0) * G + c; if (L >= nwg) return false;
;         int wgid = (int)L; { const int q = nwg / NXCD, r = nwg % NXCD, xcd = wgid % NXCD, off = wgid / NXCD; wgid = (xcd < r ? xcd * (q + 1) : r * (q + 1) + (xcd - r) * q) + off; }
;         const int tq = wgid / nN, e = tile_e[tq], ft = tile_e[256 + e] >> 8, gsz = (tile_e[320 + e] + 255) >> 8, idx = wgid - ft * nN;
;         u.pm = ft + idx % gsz; u.pn = idx / gsz; u.e = e; return true;
; __global__ void __launch_bounds__(NWAVES * 64, 2) mk_fwd(Args args) {
;     ...
;           for (int i = 0; i < 10; ++i) { pg8::Unit u; if (!S.next(i, u)) break;
;               if (tid < 256) { const int rr = u.pm * 256 + tid - pstart[u.e]; const bool valid = rr < etot[u.e]; tab[i * 256 + tid] = valid ? STOK[u.e * 8192 + rr] : 0; } }
;           __syncthreads(); }
.LBB0_2144:
	s_or_b64 exec, exec, s[26:27]
	s_add_u32 s26, s16, s81
	s_addc_u32 s27, s17, s62
	v_mov_b64_e32 v[2:3], s[10:11]
	v_cmp_ge_i64_e32 vcc, s[26:27], v[2:3]
	s_cbranch_vccnz .Ltok_flush
	s_and_saveexec_b64 s[30:31], s[2:3]
	s_cbranch_execz .LBB0_2149
	s_ashr_i32 s4, s26, 31
	s_lshr_b32 s4, s4, 29
	s_add_i32 s4, s26, s4
	s_ashr_i32 s19, s4, 3
	s_and_b32 s4, s4, -8
	s_sub_i32 s4, s26, s4
	s_lshr_b32 s20, s4, 31
	s_or_b32 s20, s63, s20
	s_mul_i32 s4, s20, s4
	s_add_i32 s4, s4, s19
	s_ashr_i32 s19, s4, 31
	s_lshr_b32 s19, s19, 28
	s_add_i32 s19, s4, s19
	s_ashr_i32 s19, s19, 4
	s_lshl_b32 s19, s19, 2
	s_add_i32 s20, 0, 0x26c00
	s_add_i32 s19, s20, s19
	v_mov_b32_e32 v2, s19
	ds_read_b32 v2, v2
	s_waitcnt lgkmcnt(0)
	v_lshlrev_b32_e32 v3, 2, v2
	v_add_u32_e32 v3, s20, v3
	ds_read2st64_b32 v[4:5], v3 offset0:4 offset1:5
	s_waitcnt lgkmcnt(0)
	v_readfirstlane_b32 s19, v5
	s_addk_i32 s19, 0xff
	s_ashr_i32 s19, s19, 8
	s_abs_i32 s19, s19
	v_cvt_f32_u32_e32 v3, s19
	v_readfirstlane_b32 s20, v4
	s_ashr_i32 s20, s20, 8
	s_sub_i32 s22, 0, s19
	v_rcp_iflag_f32_e32 v3, v3
	s_lshl_b32 s21, s20, 4
	s_sub_i32 s4, s4, s21
	s_ashr_i32 s21, s4, 31
	v_mul_f32_e32 v3, 0x4f7ffffe, v3
	v_cvt_u32_f32_e32 v3, v3
	s_abs_i32 s4, s4
	v_readfirstlane_b32 s23, v3
	s_mul_i32 s22, s22, s23
	s_mul_hi_u32 s22, s23, s22
	s_add_i32 s23, s23, s22
	s_mul_hi_u32 s22, s4, s23
	s_mul_i32 s22, s22, s19
	s_sub_i32 s4, s4, s22
	s_sub_i32 s22, s4, s19
	s_cmp_ge_u32 s4, s19
	s_cselect_b32 s4, s22, s4
	s_sub_i32 s22, s4, s19
	s_cmp_ge_u32 s4, s19
	s_cselect_b32 s4, s22, s4
	s_xor_b32 s4, s4, s21
	s_sub_i32 s4, s4, s21
	s_add_i32 s4, s4, s20
	v_lshl_add_u32 v3, s4, 8, v1
	v_sub_u32_e32 v4, v3, v4
	v_cmp_lt_i32_e32 vcc, v4, v5
	v_mov_b32_e32 v21, 0
	s_and_saveexec_b64 s[34:35], vcc
	s_cbranch_execz .LBB0_2148
	v_lshl_add_u32 v2, v2, 13, v4
	v_ashrrev_i32_e32 v3, 31, v2
	v_lshl_add_u64 v[2:3], v[2:3], 2, s[14:15]
	global_load_dword v21, v[2:3], off

;     __device__ __forceinline__ bool next(int i, Unit& u) const {
;         if (i + i0 >= imax) return false; const long L = (long)(i + i0) * G + c; if (L >= nwg) return false;
;         int wgid = (int)L; { const int q = nwg / NXCD, r = nwg % NXCD, xcd = wgid % NXCD, off = wgid / NXCD; wgid = (xcd < r ? xcd * (q + 1) : r * (q + 1) + (xcd - r) * q) + off; }
;         const int tq = wgid / nN, e = tile_e[tq], ft = tile_e[256 + e] >> 8, gsz = (tile_e[320 + e] + 255) >> 8, idx = wgid - ft * nN;
;         u.pm = ft + idx % gsz; u.pn = idx / gsz; u.e = e; return true;
; __global__ void __launch_bounds__(NWAVES * 64, 2) mk_fwd(Args args) {
;     ...
;           for (int i = 0; i < 10; ++i) { pg8::Unit u; if (!S.next(i, u)) break;
;               if (tid < 256) { const int rr = u.pm * 256 + tid - pstart[u.e]; const bool valid = rr < etot[u.e]; tab[i * 256 + tid] = valid ? STOK[u.e * 8192 + rr] : 0; } }
;           __syncthreads(); }
.LBB0_2149:
	s_or_b64 exec, exec, s[30:31]
	s_add_u32 s26, s26, s16
	s_addc_u32 s27, s27, s17
	v_mov_b64_e32 v[2:3], s[10:11]
	v_cmp_ge_i64_e32 vcc, s[26:27], v[2:3]
	s_cbranch_vccnz .Ltok_flush
	s_and_saveexec_b64 s[30:31], s[2:3]
	s_cbranch_execz .LBB0_2154
	s_ashr_i32 s4, s26, 31
	s_lshr_b32 s4, s4, 29
	s_add_i32 s4, s26, s4
	s_ashr_i32 s19, s4, 3
	s_and_b32 s4, s4, -8
	s_sub_i32 s4, s26, s4
	s_lshr_b32 s20, s4, 31
	s_or_b32 s20, s63, s20
	s_mul_i32 s4, s20, s4
	s_add_i32 s4, s4, s19
	s_ashr_i32 s19, s4, 31
	s_lshr_b32 s19, s19, 28
	s_add_i32 s19, s4, s19
	s_ashr_i32 s19, s19, 4
	s_lshl_b32 s19, s19, 2
	s_add_i32 s20, 0, 0x26c00
	s_add_i32 s19, s20, s19
	v_mov_b32_e32 v2, s19
	ds_read_b32 v2, v2
	s_waitcnt lgkmcnt(0)
	v_lshlrev_b32_e32 v3, 2, v2
	v_add_u32_e32 v3, s20, v3
	ds_read2st64_b32 v[4:5], v3 offset0:4 offset1:5
	s_waitcnt lgkmcnt(0)
	v_readfirstlane_b32 s19, v5
	s_addk_i32 s19, 0xff
	s_ashr_i32 s19, s19, 8
	s_abs_i32 s19, s19
	v_cvt_f32_u32_e32 v3, s19
	v_readfirstlane_b32 s20, v4
	s_ashr_i32 s20, s20, 8
	s_sub_i32 s22, 0, s19
	v_rcp_iflag_f32_e32 v3, v3
	s_lshl_b32 s21, s20, 4
	s_sub_i32 s4, s4, s21
	s_ashr_i32 s21, s4, 31
	v_mul_f32_e32 v3, 0x4f7ffffe, v3
	v_cvt_u32_f32_e32 v3, v3
	s_abs_i32 s4, s4
	v_readfirstlane_b32 s23, v3
	s_mul_i32 s22, s22, s23
	s_mul_hi_u32 s22, s23, s22
	s_add_i32 s23, s23, s22
	s_mul_hi_u32 s22, s4, s23
	s_mul_i32 s22, s22, s19
	s_sub_i32 s4, s4, s22
	s_sub_i32 s22, s4, s19
	s_cmp_ge_u32 s4, s19
	s_cselect_b32 s4, s22, s4
	s_sub_i32 s22, s4, s19
	s_cmp_ge_u32 s4, s19
	s_cselect_b32 s4, s22, s4
	s_xor_b32 s4, s4, s21
	s_sub_i32 s4, s4, s21
	s_add_i32 s4, s4, s20
	v_lshl_add_u32 v3, s4, 8, v1
	v_sub_u32_e32 v4, v3, v4
	v_cmp_lt_i32_e32 vcc, v4, v5
	v_mov_b32_e32 v22, 0
	s_and_saveexec_b64 s[34:35], vcc
	s_cbranch_execz .LBB0_2153
	v_lshl_add_u32 v2, v2, 13, v4
	v_ashrrev_i32_e32 v3, 31, v2
	v_lshl_add_u64 v[2:3], v[2:3], 2, s[14:15]
	global_load_dword v22, v[2:3], off

;     __device__ __forceinline__ bool next(int i, Unit& u) const {
;         if (i + i0 >= imax) return false; const long L = (long)(i + i0) * G + c; if (L >= nwg) return false;
;         int wgid = (int)L; { const int q = nwg / NXCD, r = nwg % NXCD, xcd = wgid % NXCD, off = wgid / NXCD; wgid = (xcd < r ? xcd * (q + 1) : r * (q + 1) + (xcd - r) * q) + off; }
;         const int tq = wgid / nN, e = tile_e[tq], ft = tile_e[256 + e] >> 8, gsz = (tile_e[320 + e] + 255) >> 8, idx = wgid - ft * nN;
;         u.pm = ft + idx % gsz; u.pn = idx / gsz; u.e = e; return true;
; __global__ void __launch_bounds__(NWAVES * 64, 2) mk_fwd(Args args) {
;     ...
;           for (int i = 0; i < 10; ++i) { pg8::Unit u; if (!S.next(i, u)) break;
;               if (tid < 256) { const int rr = u.pm * 256 + tid - pstart[u.e]; const bool valid = rr < etot[u.e]; tab[i * 256 + tid] = valid ? STOK[u.e * 8192 + rr] : 0; } }
;           __syncthreads(); }
.LBB0_2154:
	s_or_b64 exec, exec, s[30:31]
	s_add_u32 s26, s26, s16
	s_addc_u32 s27, s27, s17
	v_mov_b64_e32 v[2:3], s[10:11]
	v_cmp_ge_i64_e32 vcc, s[26:27], v[2:3]
	s_cbranch_vccnz .Ltok_flush
	s_and_saveexec_b64 s[30:31], s[2:3]
	s_cbranch_execz .LBB0_2159
	s_ashr_i32 s4, s26, 31
	s_lshr_b32 s4, s4, 29
	s_add_i32 s4, s26, s4
	s_ashr_i32 s19, s4, 3
	s_and_b32 s4, s4, -8
	s_sub_i32 s4, s26, s4
	s_lshr_b32 s20, s4, 31
	s_or_b32 s20, s63, s20
	s_mul_i32 s4, s20, s4
	s_add_i32 s4, s4, s19
	s_ashr_i32 s19, s4, 31
	s_lshr_b32 s19, s19, 28
	s_add_i32 s19, s4, s19
	s_ashr_i32 s19, s19, 4
	s_lshl_b32 s19, s19, 2
	s_add_i32 s20, 0, 0x26c00
	s_add_i32 s19, s20, s19
	v_mov_b32_e32 v2, s19
	ds_read_b32 v2, v2
	s_waitcnt lgkmcnt(0)
	v_lshlrev_b32_e32 v3, 2, v2
	v_add_u32_e32 v3, s20, v3
	ds_read2st64_b32 v[4:5], v3 offset0:4 offset1:5
	s_waitcnt lgkmcnt(0)
	v_readfirstlane_b32 s19, v5
	s_addk_i32 s19, 0xff
	s_ashr_i32 s19, s19, 8
	s_abs_i32 s19, s19
	v_cvt_f32_u32_e32 v3, s19
	v_readfirstlane_b32 s20, v4
	s_ashr_i32 s20, s20, 8
	s_sub_i32 s22, 0, s19
	v_rcp_iflag_f32_e32 v3, v3
	s_lshl_b32 s21, s20, 4
	s_sub_i32 s4, s4, s21
	s_ashr_i32 s21, s4, 31
	v_mul_f32_e32 v3, 0x4f7ffffe, v3
	v_cvt_u32_f32_e32 v3, v3
	s_abs_i32 s4, s4
	v_readfirstlane_b32 s23, v3
	s_mul_i32 s22, s22, s23
	s_mul_hi_u32 s22, s23, s22
	s_add_i32 s23, s23, s22
	s_mul_hi_u32 s22, s4, s23
	s_mul_i32 s22, s22, s19
	s_sub_i32 s4, s4, s22
	s_sub_i32 s22, s4, s19
	s_cmp_ge_u32 s4, s19
	s_cselect_b32 s4, s22, s4
	s_sub_i32 s22, s4, s19
	s_cmp_ge_u32 s4, s19
	s_cselect_b32 s4, s22, s4
	s_xor_b32 s4, s4, s21
	s_sub_i32 s4, s4, s21
	s_add_i32 s4, s4, s20
	v_lshl_add_u32 v3, s4, 8, v1
	v_sub_u32_e32 v4, v3, v4
	v_cmp_lt_i32_e32 vcc, v4, v5
	v_mov_b32_e32 v23, 0
	s_and_saveexec_b64 s[34:35], vcc
	s_cbranch_execz .LBB0_2158
	v_lshl_add_u32 v2, v2, 13, v4
	v_ashrrev_i32_e32 v3, 31, v2
	v_lshl_add_u64 v[2:3], v[2:3], 2, s[14:15]
	global_load_dword v23, v[2:3], off

;     __device__ __forceinline__ bool next(int i, Unit& u) const {
;         if (i + i0 >= imax) return false; const long L = (long)(i + i0) * G + c; if (L >= nwg) return false;
;         int wgid = (int)L; { const int q = nwg / NXCD, r = nwg % NXCD, xcd = wgid % NXCD, off = wgid / NXCD; wgid = (xcd < r ? xcd * (q + 1) : r * (q + 1) + (xcd - r) * q) + off; }
;         const int tq = wgid / nN, e = tile_e[tq], ft = tile_e[256 + e] >> 8, gsz = (tile_e[320 + e] + 255) >> 8, idx = wgid - ft * nN;
;         u.pm = ft + idx % gsz; u.pn = idx / gsz; u.e = e; return true;
; __global__ void __launch_bounds__(NWAVES * 64, 2) mk_fwd(Args args) {
;     ...
;           for (int i = 0; i < 10; ++i) { pg8::Unit u; if (!S.next(i, u)) break;
;               if (tid < 256) { const int rr = u.pm * 256 + tid - pstart[u.e]; const bool valid = rr < etot[u.e]; tab[i * 256 + tid] = valid ? STOK[u.e * 8192 + rr] : 0; } }
;           __syncthreads(); }
.LBB0_2159:
	s_or_b64 exec, exec, s[30:31]
	s_add_u32 s26, s26, s16
	s_addc_u32 s27, s27, s17
	v_mov_b64_e32 v[2:3], s[10:11]
	v_cmp_ge_i64_e32 vcc, s[26:27], v[2:3]
	s_cbranch_vccnz .Ltok_flush
	s_and_saveexec_b64 s[30:31], s[2:3]
	s_cbranch_execz .LBB0_2164
	s_ashr_i32 s4, s26, 31
	s_lshr_b32 s4, s4, 29
	s_add_i32 s4, s26, s4
	s_ashr_i32 s19, s4, 3
	s_and_b32 s4, s4, -8
	s_sub_i32 s4, s26, s4
	s_lshr_b32 s20, s4, 31
	s_or_b32 s20, s63, s20
	s_mul_i32 s4, s20, s4
	s_add_i32 s4, s4, s19
	s_ashr_i32 s19, s4, 31
	s_lshr_b32 s19, s19, 28
	s_add_i32 s19, s4, s19
	s_ashr_i32 s19, s19, 4
	s_lshl_b32 s19, s19, 2
	s_add_i32 s20, 0, 0x26c00
	s_add_i32 s19, s20, s19
	v_mov_b32_e32 v2, s19
	ds_read_b32 v2, v2
	s_waitcnt lgkmcnt(0)
	v_lshlrev_b32_e32 v3, 2, v2
	v_add_u32_e32 v3, s20, v3
	ds_read2st64_b32 v[4:5], v3 offset0:4 offset1:5
	s_waitcnt lgkmcnt(0)
	v_readfirstlane_b32 s19, v5
	s_addk_i32 s19, 0xff
	s_ashr_i32 s19, s19, 8
	s_abs_i32 s19, s19
	v_cvt_f32_u32_e32 v3, s19
	v_readfirstlane_b32 s20, v4
	s_ashr_i32 s20, s20, 8
	s_sub_i32 s22, 0, s19
	v_rcp_iflag_f32_e32 v3, v3
	s_lshl_b32 s21, s20, 4
	s_sub_i32 s4, s4, s21
	s_ashr_i32 s21, s4, 31
	v_mul_f32_e32 v3, 0x4f7ffffe, v3
	v_cvt_u32_f32_e32 v3, v3
	s_abs_i32 s4, s4
	v_readfirstlane_b32 s23, v3
	s_mul_i32 s22, s22, s23
	s_mul_hi_u32 s22, s23, s22
	s_add_i32 s23, s23, s22
	s_mul_hi_u32 s22, s4, s23
	s_mul_i32 s22, s22, s19
	s_sub_i32 s4, s4, s22
	s_sub_i32 s22, s4, s19
	s_cmp_ge_u32 s4, s19
	s_cselect_b32 s4, s22, s4
	s_sub_i32 s22, s4, s19
	s_cmp_ge_u32 s4, s19
	s_cselect_b32 s4, s22, s4
	s_xor_b32 s4, s4, s21
	s_sub_i32 s4, s4, s21
	s_add_i32 s4, s4, s20
	v_lshl_add_u32 v3, s4, 8, v1
	v_sub_u32_e32 v4, v3, v4
	v_cmp_lt_i32_e32 vcc, v4, v5
	v_mov_b32_e32 v24, 0
	s_and_saveexec_b64 s[34:35], vcc
	s_cbranch_execz .LBB0_2163
	v_lshl_add_u32 v2, v2, 13, v4
	v_ashrrev_i32_e32 v3, 31, v2
	v_lshl_add_u64 v[2:3], v[2:3], 2, s[14:15]
	global_load_dword v24, v[2:3], off

;     __device__ __forceinline__ bool next(int i, Unit& u) const {
;         if (i + i0 >= imax) return false; const long L = (long)(i + i0) * G + c; if (L >= nwg) return false;
;         int wgid = (int)L; { const int q = nwg / NXCD, r = nwg % NXCD, xcd = wgid % NXCD, off = wgid / NXCD; wgid = (xcd < r ? xcd * (q + 1) : r * (q + 1) + (xcd - r) * q) + off; }
;         const int tq = wgid / nN, e = tile_e[tq], ft = tile_e[256 + e] >> 8, gsz = (tile_e[320 + e] + 255) >> 8, idx = wgid - ft * nN;
;         u.pm = ft + idx % gsz; u.pn = idx / gsz; u.e = e; return true;
; __global__ void __launch_bounds__(NWAVES * 64, 2) mk_fwd(Args args) {
;     ...
;           for (int i = 0; i < 10; ++i) { pg8::Unit u; if (!S.next(i, u)) break;
;               if (tid < 256) { const int rr = u.pm * 256 + tid - pstart[u.e]; const bool valid = rr < etot[u.e]; tab[i * 256 + tid] = valid ? STOK[u.e * 8192 + rr] : 0; } }
;           __syncthreads(); }
.LBB0_2164:
	s_or_b64 exec, exec, s[30:31]
	s_add_u32 s26, s26, s16
	s_addc_u32 s27, s27, s17
	v_mov_b64_e32 v[2:3], s[10:11]
	v_cmp_ge_i64_e32 vcc, s[26:27], v[2:3]
	s_cbranch_vccnz .Ltok_flush
	s_and_saveexec_b64 s[30:31], s[2:3]
	s_cbranch_execz .LBB0_2169
	s_ashr_i32 s4, s26, 31
	s_lshr_b32 s4, s4, 29
	s_add_i32 s4, s26, s4
	s_ashr_i32 s19, s4, 3
	s_and_b32 s4, s4, -8
	s_sub_i32 s4, s26, s4
	s_lshr_b32 s20, s4, 31
	s_or_b32 s20, s63, s20
	s_mul_i32 s4, s20, s4
	s_add_i32 s4, s4, s19
	s_ashr_i32 s19, s4, 31
	s_lshr_b32 s19, s19, 28
	s_add_i32 s19, s4, s19
	s_ashr_i32 s19, s19, 4
	s_lshl_b32 s19, s19, 2
	s_add_i32 s20, 0, 0x26c00
	s_add_i32 s19, s20, s19
	v_mov_b32_e32 v2, s19
	ds_read_b32 v2, v2
	s_waitcnt lgkmcnt(0)
	v_lshlrev_b32_e32 v3, 2, v2
	v_add_u32_e32 v3, s20, v3
	ds_read2st64_b32 v[4:5], v3 offset0:4 offset1:5
	s_waitcnt lgkmcnt(0)
	v_readfirstlane_b32 s19, v5
	s_addk_i32 s19, 0xff
	s_ashr_i32 s19, s19, 8
	s_abs_i32 s19, s19
	v_cvt_f32_u32_e32 v3, s19
	v_readfirstlane_b32 s20, v4
	s_ashr_i32 s20, s20, 8
	s_sub_i32 s22, 0, s19
	v_rcp_iflag_f32_e32 v3, v3
	s_lshl_b32 s21, s20, 4
	s_sub_i32 s4, s4, s21
	s_ashr_i32 s21, s4, 31
	v_mul_f32_e32 v3, 0x4f7ffffe, v3
	v_cvt_u32_f32_e32 v3, v3
	s_abs_i32 s4, s4
	v_readfirstlane_b32 s23, v3
	s_mul_i32 s22, s22, s23
	s_mul_hi_u32 s22, s23, s22
	s_add_i32 s23, s23, s22
	s_mul_hi_u32 s22, s4, s23
	s_mul_i32 s22, s22, s19
	s_sub_i32 s4, s4, s22
	s_sub_i32 s22, s4, s19
	s_cmp_ge_u32 s4, s19
	s_cselect_b32 s4, s22, s4
	s_sub_i32 s22, s4, s19
	s_cmp_ge_u32 s4, s19
	s_cselect_b32 s4, s22, s4
	s_xor_b32 s4, s4, s21
	s_sub_i32 s4, s4, s21
	s_add_i32 s4, s4, s20
	v_lshl_add_u32 v3, s4, 8, v1
	v_sub_u32_e32 v4, v3, v4
	v_cmp_lt_i32_e32 vcc, v4, v5
	v_mov_b32_e32 v25, 0
	s_and_saveexec_b64 s[34:35], vcc
	s_cbranch_execz .LBB0_2168
	v_lshl_add_u32 v2, v2, 13, v4
	v_ashrrev_i32_e32 v3, 31, v2
	v_lshl_add_u64 v[2:3], v[2:3], 2, s[14:15]
	global_load_dword v25, v[2:3], off

;     __device__ __forceinline__ bool next(int i, Unit& u) const {
;         if (i + i0 >= imax) return false; const long L = (long)(i + i0) * G + c; if (L >= nwg) return false;
;         int wgid = (int)L; { const int q = nwg / NXCD, r = nwg % NXCD, xcd = wgid % NXCD, off = wgid / NXCD; wgid = (xcd < r ? xcd * (q + 1) : r * (q + 1) + (xcd - r) * q) + off; }
;         const int tq = wgid / nN, e = tile_e[tq], ft = tile_e[256 + e] >> 8, gsz = (tile_e[320 + e] + 255) >> 8, idx = wgid - ft * nN;
;         u.pm = ft + idx % gsz; u.pn = idx / gsz; u.e = e; return true;
; __global__ void __launch_bounds__(NWAVES * 64, 2) mk_fwd(Args args) {
;     ...
;           for (int i = 0; i < 10; ++i) { pg8::Unit u; if (!S.next(i, u)) break;
;               if (tid < 256) { const int rr = u.pm * 256 + tid - pstart[u.e]; const bool valid = rr < etot[u.e]; tab[i * 256 + tid] = valid ? STOK[u.e * 8192 + rr] : 0; } }
;           __syncthreads(); }
.LBB0_2169:
	s_or_b64 exec, exec, s[30:31]
	s_add_u32 s26, s26, s16
	s_addc_u32 s27, s27, s17
	v_mov_b64_e32 v[2:3], s[10:11]
	v_cmp_ge_i64_e32 vcc, s[26:27], v[2:3]
	s_cbranch_vccnz .Ltok_flush
	s_and_saveexec_b64 s[30:31], s[2:3]
	s_cbranch_execz .LBB0_2174
	s_ashr_i32 s4, s26, 31
	s_lshr_b32 s4, s4, 29
	s_add_i32 s4, s26, s4
	s_ashr_i32 s19, s4, 3
	s_and_b32 s4, s4, -8
	s_sub_i32 s4, s26, s4
	s_lshr_b32 s20, s4, 31
	s_or_b32 s20, s63, s20
	s_mul_i32 s4, s20, s4
	s_add_i32 s4, s4, s19
	s_ashr_i32 s19, s4, 31
	s_lshr_b32 s19, s19, 28
	s_add_i32 s19, s4, s19
	s_ashr_i32 s19, s19, 4
	s_lshl_b32 s19, s19, 2
	s_add_i32 s20, 0, 0x26c00
	s_add_i32 s19, s20, s19
	v_mov_b32_e32 v2, s19
	ds_read_b32 v2, v2
	s_waitcnt lgkmcnt(0)
	v_lshlrev_b32_e32 v3, 2, v2
	v_add_u32_e32 v3, s20, v3
	ds_read2st64_b32 v[4:5], v3 offset0:4 offset1:5
	s_waitcnt lgkmcnt(0)
	v_readfirstlane_b32 s19, v5
	s_addk_i32 s19, 0xff
	s_ashr_i32 s19, s19, 8
	s_abs_i32 s19, s19
	v_cvt_f32_u32_e32 v3, s19
	v_readfirstlane_b32 s20, v4
	s_ashr_i32 s20, s20, 8
	s_sub_i32 s22, 0, s19
	v_rcp_iflag_f32_e32 v3, v3
	s_lshl_b32 s21, s20, 4
	s_sub_i32 s4, s4, s21
	s_ashr_i32 s21, s4, 31
	v_mul_f32_e32 v3, 0x4f7ffffe, v3
	v_cvt_u32_f32_e32 v3, v3
	s_abs_i32 s4, s4
	v_readfirstlane_b32 s23, v3
	s_mul_i32 s22, s22, s23
	s_mul_hi_u32 s22, s23, s22
	s_add_i32 s23, s23, s22
	s_mul_hi_u32 s22, s4, s23
	s_mul_i32 s22, s22, s19
	s_sub_i32 s4, s4, s22
	s_sub_i32 s22, s4, s19
	s_cmp_ge_u32 s4, s19
	s_cselect_b32 s4, s22, s4
	s_sub_i32 s22, s4, s19
	s_cmp_ge_u32 s4, s19
	s_cselect_b32 s4, s22, s4
	s_xor_b32 s4, s4, s21
	s_sub_i32 s4, s4, s21
	s_add_i32 s4, s4, s20
	v_lshl_add_u32 v3, s4, 8, v1
	v_sub_u32_e32 v4, v3, v4
	v_cmp_lt_i32_e32 vcc, v4, v5
	v_mov_b32_e32 v26, 0
	s_and_saveexec_b64 s[34:35], vcc
	s_cbranch_execz .LBB0_2173
	v_lshl_add_u32 v2, v2, 13, v4
	v_ashrrev_i32_e32 v3, 31, v2
	v_lshl_add_u64 v[2:3], v[2:3], 2, s[14:15]
	global_load_dword v26, v[2:3], off

;     __device__ __forceinline__ bool next(int i, Unit& u) const {
;         if (i + i0 >= imax) return false; const long L = (long)(i + i0) * G + c; if (L >= nwg) return false;
;         int wgid = (int)L; { const int q = nwg / NXCD, r = nwg % NXCD, xcd = wgid % NXCD, off = wgid / NXCD; wgid = (xcd < r ? xcd * (q + 1) : r * (q + 1) + (xcd - r) * q) + off; }
;         const int tq = wgid / nN, e = tile_e[tq], ft = tile_e[256 + e] >> 8, gsz = (tile_e[320 + e] + 255) >> 8, idx = wgid - ft * nN;
;         u.pm = ft + idx % gsz; u.pn = idx / gsz; u.e = e; return true;
; __global__ void __launch_bounds__(NWAVES * 64, 2) mk_fwd(Args args) {
;     ...
;           for (int i = 0; i < 10; ++i) { pg8::Unit u; if (!S.next(i, u)) break;
;               if (tid < 256) { const int rr = u.pm * 256 + tid - pstart[u.e]; const bool valid = rr < etot[u.e]; tab[i * 256 + tid] = valid ? STOK[u.e * 8192 + rr] : 0; } }
;           __syncthreads(); }
.LBB0_2174:
	s_or_b64 exec, exec, s[30:31]
	s_add_u32 s26, s26, s16
	s_addc_u32 s27, s27, s17
	v_mov_b64_e32 v[2:3], s[10:11]
	v_cmp_ge_i64_e32 vcc, s[26:27], v[2:3]
	s_cbranch_vccnz .Ltok_flush
	s_and_saveexec_b64 s[30:31], s[2:3]
	s_cbranch_execz .LBB0_2179
	s_ashr_i32 s4, s26, 31
	s_lshr_b32 s4, s4, 29
	s_add_i32 s4, s26, s4
	s_ashr_i32 s19, s4, 3
	s_and_b32 s4, s4, -8
	s_sub_i32 s4, s26, s4
	s_lshr_b32 s20, s4, 31
	s_or_b32 s20, s63, s20
	s_mul_i32 s4, s20, s4
	s_add_i32 s4, s4, s19
	s_ashr_i32 s19, s4, 31
	s_lshr_b32 s19, s19, 28
	s_add_i32 s19, s4, s19
	s_ashr_i32 s19, s19, 4
	s_lshl_b32 s19, s19, 2
	s_add_i32 s20, 0, 0x26c00
	s_add_i32 s19, s20, s19
	v_mov_b32_e32 v2, s19
	ds_read_b32 v2, v2
	s_waitcnt lgkmcnt(0)
	v_lshlrev_b32_e32 v3, 2, v2
	v_add_u32_e32 v3, s20, v3
	ds_read2st64_b32 v[4:5], v3 offset0:4 offset1:5
	s_waitcnt lgkmcnt(0)
	v_readfirstlane_b32 s19, v5
	s_addk_i32 s19, 0xff
	s_ashr_i32 s19, s19, 8
	s_abs_i32 s19, s19
	v_cvt_f32_u32_e32 v3, s19
	v_readfirstlane_b32 s20, v4
	s_ashr_i32 s20, s20, 8
	s_sub_i32 s22, 0, s19
	v_rcp_iflag_f32_e32 v3, v3
	s_lshl_b32 s21, s20, 4
	s_sub_i32 s4, s4, s21
	s_ashr_i32 s21, s4, 31
	v_mul_f32_e32 v3, 0x4f7ffffe, v3
	v_cvt_u32_f32_e32 v3, v3
	s_abs_i32 s4, s4
	v_readfirstlane_b32 s23, v3
	s_mul_i32 s22, s22, s23
	s_mul_hi_u32 s22, s23, s22
	s_add_i32 s23, s23, s22
	s_mul_hi_u32 s22, s4, s23
	s_mul_i32 s22, s22, s19
	s_sub_i32 s4, s4, s22
	s_sub_i32 s22, s4, s19
	s_cmp_ge_u32 s4, s19
	s_cselect_b32 s4, s22, s4
	s_sub_i32 s22, s4, s19
	s_cmp_ge_u32 s4, s19
	s_cselect_b32 s4, s22, s4
	s_xor_b32 s4, s4, s21
	s_sub_i32 s4, s4, s21
	s_add_i32 s4, s4, s20
	v_lshl_add_u32 v3, s4, 8, v1
	v_sub_u32_e32 v4, v3, v4
	v_cmp_lt_i32_e32 vcc, v4, v5
	v_mov_b32_e32 v27, 0
	s_and_saveexec_b64 s[34:35], vcc
	s_cbranch_execz .LBB0_2178
	v_lshl_add_u32 v2, v2, 13, v4
	v_ashrrev_i32_e32 v3, 31, v2
	v_lshl_add_u64 v[2:3], v[2:3], 2, s[14:15]
	global_load_dword v27, v[2:3], off

;     __device__ __forceinline__ bool next(int i, Unit& u) const {
;         if (i + i0 >= imax) return false; const long L = (long)(i + i0) * G + c; if (L >= nwg) return false;
;         int wgid = (int)L; { const int q = nwg / NXCD, r = nwg % NXCD, xcd = wgid % NXCD, off = wgid / NXCD; wgid = (xcd < r ? xcd * (q + 1) : r * (q + 1) + (xcd - r) * q) + off; }
;         const int tq = wgid / nN, e = tile_e[tq], ft = tile_e[256 + e] >> 8, gsz = (tile_e[320 + e] + 255) >> 8, idx = wgid - ft * nN;
;         u.pm = ft + idx % gsz; u.pn = idx / gsz; u.e = e; return true;
; __global__ void __launch_bounds__(NWAVES * 64, 2) mk_fwd(Args args) {
;     ...
;           for (int i = 0; i < 10; ++i) { pg8::Unit u; if (!S.next(i, u)) break;
;               if (tid < 256) { const int rr = u.pm * 256 + tid - pstart[u.e]; const bool valid = rr < etot[u.e]; tab[i * 256 + tid] = valid ? STOK[u.e * 8192 + rr] : 0; } }
;           __syncthreads(); }
.LBB0_2179:
	s_or_b64 exec, exec, s[30:31]
	s_add_u32 s26, s26, s16
	s_addc_u32 s27, s27, s17
	v_mov_b64_e32 v[2:3], s[10:11]
	v_cmp_ge_i64_e32 vcc, s[26:27], v[2:3]
	s_cbranch_vccnz .Ltok_flush
	s_and_saveexec_b64 s[30:31], s[2:3]
	s_cbranch_execz .LBB0_2184
	s_ashr_i32 s4, s26, 31
	s_lshr_b32 s4, s4, 29
	s_add_i32 s4, s26, s4
	s_ashr_i32 s19, s4, 3
	s_and_b32 s4, s4, -8
	s_sub_i32 s4, s26, s4
	s_lshr_b32 s20, s4, 31
	s_or_b32 s20, s63, s20
	s_mul_i32 s4, s20, s4
	s_add_i32 s4, s4, s19
	s_ashr_i32 s19, s4, 31
	s_lshr_b32 s19, s19, 28
	s_add_i32 s19, s4, s19
	s_ashr_i32 s19, s19, 4
	s_lshl_b32 s19, s19, 2
	s_add_i32 s20, 0, 0x26c00
	s_add_i32 s19, s20, s19
	v_mov_b32_e32 v2, s19
	ds_read_b32 v2, v2
	s_waitcnt lgkmcnt(0)
	v_lshlrev_b32_e32 v3, 2, v2
	v_add_u32_e32 v3, s20, v3
	ds_read2st64_b32 v[4:5], v3 offset0:4 offset1:5
	s_waitcnt lgkmcnt(0)
	v_readfirstlane_b32 s19, v5
	s_addk_i32 s19, 0xff
	s_ashr_i32 s19, s19, 8
	s_abs_i32 s19, s19
	v_cvt_f32_u32_e32 v3, s19
	v_readfirstlane_b32 s20, v4
	s_ashr_i32 s20, s20, 8
	s_sub_i32 s22, 0, s19
	v_rcp_iflag_f32_e32 v3, v3
	s_lshl_b32 s21, s20, 4
	s_sub_i32 s4, s4, s21
	s_ashr_i32 s21, s4, 31
	v_mul_f32_e32 v3, 0x4f7ffffe, v3
	v_cvt_u32_f32_e32 v3, v3
	s_abs_i32 s4, s4
	v_readfirstlane_b32 s23, v3
	s_mul_i32 s22, s22, s23
	s_mul_hi_u32 s22, s23, s22
	s_add_i32 s23, s23, s22
	s_mul_hi_u32 s22, s4, s23
	s_mul_i32 s22, s22, s19
	s_sub_i32 s4, s4, s22
	s_sub_i32 s22, s4, s19
	s_cmp_ge_u32 s4, s19
	s_cselect_b32 s4, s22, s4
	s_sub_i32 s22, s4, s19
	s_cmp_ge_u32 s4, s19
	s_cselect_b32 s4, s22, s4
	s_xor_b32 s4, s4, s21
	s_sub_i32 s4, s4, s21
	s_add_i32 s4, s4, s20
	v_lshl_add_u32 v3, s4, 8, v1
	v_sub_u32_e32 v4, v3, v4
	v_cmp_lt_i32_e32 vcc, v4, v5
	v_mov_b32_e32 v28, 0
	s_and_saveexec_b64 s[34:35], vcc
	s_cbranch_execz .LBB0_2183
	v_lshl_add_u32 v2, v2, 13, v4
	v_ashrrev_i32_e32 v3, 31, v2
	v_lshl_add_u64 v[2:3], v[2:3], 2, s[14:15]
	global_load_dword v28, v[2:3], off

; __global__ void __launch_bounds__(NWAVES * 64, 2) mk_fwd(Args args) {
;     ...
;           for (int i = 0; i < 10; ++i) { pg8::Unit u; if (!S.next(i, u)) break;
;               if (tid < 256) { const int rr = u.pm * 256 + tid - pstart[u.e]; const bool valid = rr < etot[u.e]; tab[i * 256 + tid] = valid ? STOK[u.e * 8192 + rr] : 0; } }
;           __syncthreads(); }
.LBB0_2184:
	s_or_b64 exec, exec, s[30:31]
	s_add_u32 s30, s26, s16
	s_addc_u32 s31, s27, s17
	v_mov_b64_e32 v[2:3], s[10:11]
	v_cmp_ge_i64_e32 vcc, s[30:31], v[2:3]
	s_cbranch_vccnz .Ltok_flush
	s_and_saveexec_b64 s[26:27], s[2:3]
	s_cbranch_execz .LBB0_2189
	s_ashr_i32 s2, s30, 31
	s_lshr_b32 s2, s2, 29
	s_add_i32 s2, s30, s2
	s_ashr_i32 s3, s2, 3
	s_and_b32 s2, s2, -8
	s_sub_i32 s2, s30, s2
	s_lshr_b32 s4, s2, 31
	s_or_b32 s4, s63, s4
	s_mul_i32 s2, s4, s2
	s_add_i32 s2, s2, s3
	s_ashr_i32 s3, s2, 31
	s_lshr_b32 s3, s3, 28
	s_add_i32 s3, s2, s3
	s_ashr_i32 s3, s3, 4
	s_lshl_b32 s3, s3, 2
	s_add_i32 s4, 0, 0x26c00
	s_add_i32 s3, s4, s3
	v_mov_b32_e32 v2, s3
	ds_read_b32 v2, v2
	s_waitcnt lgkmcnt(0)
	v_lshlrev_b32_e32 v3, 2, v2
	v_add_u32_e32 v3, s4, v3
	ds_read2st64_b32 v[4:5], v3 offset0:4 offset1:5
	s_waitcnt lgkmcnt(0)
	v_readfirstlane_b32 s3, v5
	s_addk_i32 s3, 0xff
	s_ashr_i32 s3, s3, 8
	s_abs_i32 s3, s3
	v_cvt_f32_u32_e32 v3, s3
	v_readfirstlane_b32 s4, v4
	s_ashr_i32 s4, s4, 8
	s_sub_i32 s20, 0, s3
	v_rcp_iflag_f32_e32 v3, v3
	s_lshl_b32 s19, s4, 4
	s_sub_i32 s2, s2, s19
	s_ashr_i32 s19, s2, 31
	v_mul_f32_e32 v3, 0x4f7ffffe, v3
	v_cvt_u32_f32_e32 v3, v3
	s_abs_i32 s2, s2
	v_readfirstlane_b32 s21, v3
	s_mul_i32 s20, s20, s21
	s_mul_hi_u32 s20, s21, s20
	s_add_i32 s21, s21, s20
	s_mul_hi_u32 s20, s2, s21
	s_mul_i32 s20, s20, s3
	s_sub_i32 s2, s2, s20
	s_sub_i32 s20, s2, s3
	s_cmp_ge_u32 s2, s3
	s_cselect_b32 s2, s20, s2
	s_sub_i32 s20, s2, s3
	s_cmp_ge_u32 s2, s3
	s_cselect_b32 s2, s20, s2
	s_xor_b32 s2, s2, s19
	s_sub_i32 s2, s2, s19
	s_add_i32 s2, s2, s4
	v_lshl_add_u32 v1, s2, 8, v1
	v_sub_u32_e32 v3, v1, v4
	v_cmp_lt_i32_e32 vcc, v3, v5
	v_mov_b32_e32 v29, 0
	s_and_saveexec_b64 s[2:3], vcc
	s_cbranch_execz .LBB0_2188
	v_lshl_add_u32 v2, v2, 13, v3
	v_ashrrev_i32_e32 v3, 31, v2
	v_lshl_add_u64 v[2:3], v[2:3], 2, s[14:15]
	global_load_dword v29, v[2:3], off
.LBB0_2188:
	s_or_b64 exec, exec, s[2:3]
.LBB0_2189:
	s_or_b64 exec, exec, s[26:27]
.Ltok_flush:
	s_waitcnt vmcnt(0)
	s_and_saveexec_b64 s[24:25], s[2:3]
	ds_write_b32 v0, v20
	ds_write_b32 v0, v21 offset:1024
	ds_write_b32 v0, v22 offset:2048
	ds_write_b32 v0, v23 offset:3072
	ds_write_b32 v0, v24 offset:4096
	ds_write_b32 v0, v25 offset:5120
	ds_write_b32 v0, v26 offset:6144
	ds_write_b32 v0, v27 offset:7168
	ds_write_b32 v0, v28 offset:8192
	ds_write_b32 v0, v29 offset:9216
	s_or_b64 exec, exec, s[24:25]
